# grid barrier: all waiters poll the cross-XCC arrival counter directly (no generation word bump after the last leader's atomic)
# speedup vs baseline: 1.0262x; 1.0009x over previous
.LBB0_240:
	v_readlane_b32 s4, v245, 22
	v_readlane_b32 s5, v245, 23
	v_cvt_f32_u32_e32 v1, v3
	v_sub_u32_e32 v5, 0, v3
	v_rcp_iflag_f32_e32 v1, v1
	s_nop 1
	global_atomic_add v4, v195, v203, s[4:5] sc0
	v_mul_f32_e32 v1, 0x4f7ffffe, v1
	v_cvt_u32_f32_e32 v1, v1
	v_mul_lo_u32 v5, v5, v1
	v_mul_hi_u32 v5, v1, v5
	v_add_u32_e32 v1, v1, v5
	s_waitcnt vmcnt(0)
	v_mul_hi_u32 v1, v4, v1
	v_mul_lo_u32 v5, v1, v3
	v_sub_u32_e32 v5, v4, v5
	v_add_u32_e32 v6, 1, v1
	v_cmp_ge_u32_e32 vcc, v5, v3
	v_add_u32_e32 v4, 1, v4
	s_nop 0
	v_cndmask_b32_e32 v1, v1, v6, vcc
	v_sub_u32_e32 v6, v5, v3
	v_cndmask_b32_e32 v5, v5, v6, vcc
	v_add_u32_e32 v6, 1, v1
	v_cmp_ge_u32_e32 vcc, v5, v3
	s_nop 1
	v_cndmask_b32_e32 v1, v1, v6, vcc
	v_mul_lo_u32 v5, v3, v1
	v_add_u32_e32 v3, v5, v3
	v_cmp_ne_u32_e32 vcc, v4, v3
	s_and_saveexec_b64 s[4:5], vcc
	s_xor_b64 s[4:5], exec, s[4:5]
	s_cbranch_execz .LBB0_254
	buffer_inv sc1
	v_readlane_b32 s6, v245, 26
	v_readlane_b32 s7, v245, 27
	s_waitcnt lgkmcnt(0)
	v_mad_u32_u24 v6, v1, v2, v2
	s_nop 3
	global_load_dword v2, v195, s[6:7] sc1
	s_waitcnt vmcnt(0)
	v_cmp_lt_u32_e32 vcc, v2, v6
	s_and_saveexec_b64 s[6:7], vcc
	s_cbranch_execz .LBB0_253
	s_mov_b32 s19, 1
	s_mov_b64 s[8:9], 0
	s_branch .LBB0_244

.LBB0_248:
	v_readlane_b32 s12, v245, 26
	v_readlane_b32 s13, v245, 27
	s_add_i32 s19, s19, 1
	s_mov_b64 s[14:15], -1
	s_nop 2
	global_load_dword v2, v195, s[12:13] sc1
	s_waitcnt vmcnt(0)
	v_cmp_ge_u32_e32 vcc, v2, v6
	s_orn2_b64 s[12:13], vcc, exec
	s_branch .LBB0_243

.LBB0_257:
	s_or_b64 exec, exec, s[6:7]
	s_waitcnt vmcnt(0)
	v_readfirstlane_b32 s4, v3
	v_sub_u32_e32 v4, 0, v2
	s_mov_b64 s[6:7], -1
	v_add_u32_e32 v3, s4, v1
	v_cvt_f32_u32_e32 v1, v2
	v_readlane_b32 s4, v245, 28
	v_readlane_b32 s5, v245, 29
	v_rcp_iflag_f32_e32 v1, v1
	s_nop 0
	v_mul_f32_e32 v1, 0x4f7ffffe, v1
	v_cvt_u32_f32_e32 v1, v1
	v_mul_lo_u32 v4, v4, v1
	v_mul_hi_u32 v4, v1, v4
	v_add_u32_e32 v1, v1, v4
	v_mul_hi_u32 v1, v3, v1
	v_mul_lo_u32 v4, v1, v2
	v_sub_u32_e32 v4, v3, v4
	v_cmp_ge_u32_e32 vcc, v4, v2
	v_add_u32_e32 v5, 1, v1
	v_add_u32_e32 v3, 1, v3
	v_cndmask_b32_e32 v1, v1, v5, vcc
	v_sub_u32_e32 v5, v4, v2
	v_cndmask_b32_e32 v4, v4, v5, vcc
	v_cmp_ge_u32_e32 vcc, v4, v2
	v_add_u32_e32 v4, 1, v1
	s_nop 0
	v_cndmask_b32_e32 v1, v1, v4, vcc
	v_mul_lo_u32 v4, v2, v1
	v_add_u32_e32 v2, v4, v2
	v_mov_b32_e32 v6, v2
	v_cmp_ne_u32_e32 vcc, v3, v2
	v_mov_b64_e32 v[2:3], s[4:5]
	s_and_saveexec_b64 s[4:5], vcc
	s_cbranch_execz .LBB0_269
	v_readlane_b32 s6, v245, 26
	v_readlane_b32 s7, v245, 27
	s_mov_b64 s[8:9], 0
	s_nop 3
	global_load_dword v2, v195, s[6:7] sc1
	s_waitcnt vmcnt(0)
	v_cmp_lt_u32_e32 vcc, v2, v6
	s_and_saveexec_b64 s[6:7], vcc
	s_cbranch_execz .LBB0_268
	s_mov_b32 s19, 1
	s_branch .LBB0_261

.LBB0_518:
	v_readlane_b32 s4, v245, 22
	v_readlane_b32 s5, v245, 23
	v_cvt_f32_u32_e32 v1, v3
	v_sub_u32_e32 v5, 0, v3
	v_rcp_iflag_f32_e32 v1, v1
	s_nop 1
	global_atomic_add v4, v195, v203, s[4:5] sc0
	v_mul_f32_e32 v1, 0x4f7ffffe, v1
	v_cvt_u32_f32_e32 v1, v1
	v_mul_lo_u32 v5, v5, v1
	v_mul_hi_u32 v5, v1, v5
	v_add_u32_e32 v1, v1, v5
	s_waitcnt vmcnt(0)
	v_mul_hi_u32 v1, v4, v1
	v_mul_lo_u32 v5, v1, v3
	v_sub_u32_e32 v5, v4, v5
	v_add_u32_e32 v6, 1, v1
	v_cmp_ge_u32_e32 vcc, v5, v3
	v_add_u32_e32 v4, 1, v4
	s_nop 0
	v_cndmask_b32_e32 v1, v1, v6, vcc
	v_sub_u32_e32 v6, v5, v3
	v_cndmask_b32_e32 v5, v5, v6, vcc
	v_add_u32_e32 v6, 1, v1
	v_cmp_ge_u32_e32 vcc, v5, v3
	s_nop 1
	v_cndmask_b32_e32 v1, v1, v6, vcc
	v_mul_lo_u32 v5, v3, v1
	v_add_u32_e32 v3, v5, v3
	v_cmp_ne_u32_e32 vcc, v4, v3
	s_and_saveexec_b64 s[4:5], vcc
	s_xor_b64 s[4:5], exec, s[4:5]
	s_cbranch_execz .LBB0_532
	buffer_inv sc1
	v_readlane_b32 s6, v245, 26
	v_readlane_b32 s7, v245, 27
	s_waitcnt lgkmcnt(0)
	v_mad_u32_u24 v6, v1, v2, v2
	s_nop 3
	global_load_dword v2, v195, s[6:7] sc1
	s_waitcnt vmcnt(0)
	v_cmp_lt_u32_e32 vcc, v2, v6
	s_and_saveexec_b64 s[6:7], vcc
	s_cbranch_execz .LBB0_531
	s_mov_b32 s18, 1
	s_mov_b64 s[8:9], 0
	s_branch .LBB0_522

.LBB0_526:
	v_readlane_b32 s12, v245, 26
	v_readlane_b32 s13, v245, 27
	s_add_i32 s18, s18, 1
	s_mov_b64 s[14:15], -1
	s_nop 2
	global_load_dword v2, v195, s[12:13] sc1
	s_waitcnt vmcnt(0)
	v_cmp_ge_u32_e32 vcc, v2, v6
	s_orn2_b64 s[12:13], vcc, exec
	s_branch .LBB0_521

.LBB0_535:
	s_or_b64 exec, exec, s[6:7]
	s_waitcnt vmcnt(0)
	v_readfirstlane_b32 s4, v3
	v_sub_u32_e32 v4, 0, v2
	s_mov_b64 s[6:7], -1
	v_add_u32_e32 v3, s4, v1
	v_cvt_f32_u32_e32 v1, v2
	v_readlane_b32 s4, v245, 28
	v_readlane_b32 s5, v245, 29
	v_rcp_iflag_f32_e32 v1, v1
	s_nop 0
	v_mul_f32_e32 v1, 0x4f7ffffe, v1
	v_cvt_u32_f32_e32 v1, v1
	v_mul_lo_u32 v4, v4, v1
	v_mul_hi_u32 v4, v1, v4
	v_add_u32_e32 v1, v1, v4
	v_mul_hi_u32 v1, v3, v1
	v_mul_lo_u32 v4, v1, v2
	v_sub_u32_e32 v4, v3, v4
	v_cmp_ge_u32_e32 vcc, v4, v2
	v_add_u32_e32 v5, 1, v1
	v_add_u32_e32 v3, 1, v3
	v_cndmask_b32_e32 v1, v1, v5, vcc
	v_sub_u32_e32 v5, v4, v2
	v_cndmask_b32_e32 v4, v4, v5, vcc
	v_cmp_ge_u32_e32 vcc, v4, v2
	v_add_u32_e32 v4, 1, v1
	s_nop 0
	v_cndmask_b32_e32 v1, v1, v4, vcc
	v_mul_lo_u32 v4, v2, v1
	v_add_u32_e32 v2, v4, v2
	v_mov_b32_e32 v6, v2
	v_cmp_ne_u32_e32 vcc, v3, v2
	v_mov_b64_e32 v[2:3], s[4:5]
	s_and_saveexec_b64 s[4:5], vcc
	s_cbranch_execz .LBB0_547
	v_readlane_b32 s6, v245, 26
	v_readlane_b32 s7, v245, 27
	s_mov_b64 s[8:9], 0
	s_nop 3
	global_load_dword v2, v195, s[6:7] sc1
	s_waitcnt vmcnt(0)
	v_cmp_lt_u32_e32 vcc, v2, v6
	s_and_saveexec_b64 s[6:7], vcc
	s_cbranch_execz .LBB0_546
	s_mov_b32 s18, 1
	s_branch .LBB0_539

.LBB0_879:
	s_or_b64 exec, exec, s[6:7]
	s_waitcnt vmcnt(0)
	v_readfirstlane_b32 s4, v3
	v_sub_u32_e32 v4, 0, v2
	s_mov_b64 s[6:7], -1
	v_add_u32_e32 v3, s4, v1
	v_cvt_f32_u32_e32 v1, v2
	v_readlane_b32 s4, v245, 28
	v_readlane_b32 s5, v245, 29
	v_rcp_iflag_f32_e32 v1, v1
	s_nop 0
	v_mul_f32_e32 v1, 0x4f7ffffe, v1
	v_cvt_u32_f32_e32 v1, v1
	v_mul_lo_u32 v4, v4, v1
	v_mul_hi_u32 v4, v1, v4
	v_add_u32_e32 v1, v1, v4
	v_mul_hi_u32 v1, v3, v1
	v_mul_lo_u32 v4, v1, v2
	v_sub_u32_e32 v4, v3, v4
	v_cmp_ge_u32_e32 vcc, v4, v2
	v_add_u32_e32 v5, 1, v1
	v_add_u32_e32 v3, 1, v3
	v_cndmask_b32_e32 v1, v1, v5, vcc
	v_sub_u32_e32 v5, v4, v2
	v_cndmask_b32_e32 v4, v4, v5, vcc
	v_cmp_ge_u32_e32 vcc, v4, v2
	v_add_u32_e32 v4, 1, v1
	s_nop 0
	v_cndmask_b32_e32 v1, v1, v4, vcc
	v_mul_lo_u32 v4, v2, v1
	v_add_u32_e32 v2, v4, v2
	v_mov_b32_e32 v6, v2
	v_cmp_ne_u32_e32 vcc, v3, v2
	v_mov_b64_e32 v[2:3], s[4:5]
	s_and_saveexec_b64 s[4:5], vcc
	s_cbranch_execnz .LBB0_880
	s_getpc_b64 s[98:99]

.LBB0_880:
	v_readlane_b32 s6, v245, 26
	v_readlane_b32 s7, v245, 27
	s_mov_b64 s[8:9], 0
	s_nop 3
	global_load_dword v2, v195, s[6:7] sc1
	s_waitcnt vmcnt(0)
	v_cmp_lt_u32_e32 vcc, v2, v6
	s_and_saveexec_b64 s[6:7], vcc
	s_cbranch_execnz .LBB0_881
	s_getpc_b64 s[98:99]
